# fused GEMM epilogues: the 16 residual loads issued after the panel-arrival atomic instead of before the row statistics (arrival no longer waits for them)
# speedup vs baseline: 1.0059x; 1.0059x over previous
.LBB0_594:
	s_lshl_b32 s4, s21, 5
	s_lshl_b32 s5, s20, 8
	v_lshrrev_b32_e32 v0, 1, v166
	s_or_b32 s4, s5, s4
	v_and_or_b32 v220, v0, 24, s4
	s_lshl_b32 s37, s83, 8
	v_add_u32_e32 v118, s37, v240
	v_ashrrev_i32_e32 v221, 31, v220
	v_lshl_add_u64 v[120:121], v[220:221], 1, s[6:7]
	s_mov_b64 s[4:5], 0x4000000
	v_ashrrev_i32_e32 v119, 31, v118
	v_lshl_add_u64 v[120:121], v[120:121], 0, s[4:5]
	v_lshlrev_b64 v[224:225], 11, v[118:119]
	v_lshl_add_u64 v[126:127], v[120:121], 0, v[224:225]
	s_barrier
	v_and_b32_e32 v168, 64, v231
	v_xor_b32_e32 v0, 16, v231
	v_add_u32_e32 v168, 64, v168
	v_cmp_lt_i32_e32 vcc, v0, v168
	v_mul_f32_e32 v169, v137, v137
	v_fmac_f32_e32 v169, v136, v136
	v_cndmask_b32_e32 v0, v231, v0, vcc
	v_lshlrev_b32_e32 v241, 2, v0
	v_mul_f32_e32 v0, v135, v135
	v_fmac_f32_e32 v0, v134, v134
	v_add_f32_e32 v0, v0, v169
	v_mul_f32_e32 v169, v131, v131
	v_mul_f32_e32 v170, v133, v133
	v_fmac_f32_e32 v169, v130, v130
	v_fmac_f32_e32 v170, v132, v132
	v_add_f32_e32 v169, v169, v170
	v_add_f32_e32 v0, v169, v0
	v_mul_f32_e32 v169, v123, v123
	v_mul_f32_e32 v170, v125, v125
	v_fmac_f32_e32 v169, v122, v122
	v_fmac_f32_e32 v170, v124, v124
	v_add_f32_e32 v169, v169, v170
	v_add_f32_e32 v0, v169, v0
	v_mul_f32_e32 v169, v115, v115
	v_mul_f32_e32 v170, v117, v117
	v_fmac_f32_e32 v169, v114, v114
	v_fmac_f32_e32 v170, v116, v116
	v_add_f32_e32 v169, v169, v170
	v_add_f32_e32 v0, v169, v0
	ds_bpermute_b32 v169, v241, v0
	v_xor_b32_e32 v170, 32, v231
	v_cmp_lt_i32_e32 vcc, v170, v168
	s_lshl_b32 s4, s21, 2
	s_add_i32 s36, s4, 0
	v_cndmask_b32_e32 v168, v231, v170, vcc
	v_lshlrev_b32_e32 v242, 2, v168
	s_waitcnt lgkmcnt(0)
	v_add_f32_e32 v168, v0, v169
	ds_bpermute_b32 v169, v242, v168
	v_and_b32_e32 v0, 63, v166
	v_cmp_gt_u32_e64 s[42:43], 16, v0
	s_and_saveexec_b64 s[6:7], s[42:43]
	s_load_dwordx2 s[90:91], s[0:1], 0xb0
	v_readlane_b32 s64, v252, 3
	v_readlane_b32 s65, v255, 10
	v_readlane_b32 s68, v255, 11
	v_readlane_b32 s74, v255, 12
	v_readlane_b32 s95, v255, 13
	s_movk_i32 s92, 0x2b20
	s_cbranch_execz .LBB0_596
	s_lshl_b32 s4, s82, 10
	s_add_i32 s4, s36, s4
	s_waitcnt lgkmcnt(0)
	v_add_f32_e32 v168, v168, v169
	v_lshl_add_u32 v169, v167, 4, s4
	ds_write_b32 v169, v168

.LBB0_615:
	s_or_b64 exec, exec, s[8:9]
	global_load_dwordx4 v[206:209], v[126:127], off
	global_load_dwordx4 v[202:205], v[126:127], off offset:256
	v_or_b32_e32 v126, 16, v118
	v_ashrrev_i32_e32 v127, 31, v126
	v_lshlrev_b64 v[126:127], 11, v[126:127]
	v_lshl_add_u64 v[126:127], v[120:121], 0, v[126:127]
	global_load_dwordx4 v[198:201], v[126:127], off
	global_load_dwordx4 v[194:197], v[126:127], off offset:256
	v_or_b32_e32 v126, 32, v118
	v_ashrrev_i32_e32 v127, 31, v126
	v_lshlrev_b64 v[126:127], 11, v[126:127]
	v_lshl_add_u64 v[126:127], v[120:121], 0, v[126:127]
	global_load_dwordx4 v[190:193], v[126:127], off
	global_load_dwordx4 v[186:189], v[126:127], off offset:256
	v_or_b32_e32 v126, 48, v118
	v_ashrrev_i32_e32 v127, 31, v126
	v_lshlrev_b64 v[126:127], 11, v[126:127]
	v_lshl_add_u64 v[126:127], v[120:121], 0, v[126:127]
	global_load_dwordx4 v[174:177], v[126:127], off
	global_load_dwordx4 v[162:165], v[126:127], off offset:256
	v_add_u32_e32 v126, 0x80, v118
	v_ashrrev_i32_e32 v127, 31, v126
	v_lshlrev_b64 v[126:127], 11, v[126:127]
	v_lshl_add_u64 v[126:127], v[120:121], 0, v[126:127]
	global_load_dwordx4 v[158:161], v[126:127], off
	global_load_dwordx4 v[154:157], v[126:127], off offset:256
	v_add_u32_e32 v126, 0x90, v118
	v_ashrrev_i32_e32 v127, 31, v126
	v_lshlrev_b64 v[126:127], 11, v[126:127]
	v_lshl_add_u64 v[126:127], v[120:121], 0, v[126:127]
	global_load_dwordx4 v[150:153], v[126:127], off
	global_load_dwordx4 v[146:149], v[126:127], off offset:256
	v_add_u32_e32 v126, 0xa0, v118
	v_add_u32_e32 v118, 0xb0, v118
	v_ashrrev_i32_e32 v127, 31, v126
	v_ashrrev_i32_e32 v119, 31, v118
	v_lshlrev_b64 v[126:127], 11, v[126:127]
	v_lshlrev_b64 v[118:119], 11, v[118:119]
	v_lshl_add_u64 v[126:127], v[120:121], 0, v[126:127]
	v_lshl_add_u64 v[118:119], v[120:121], 0, v[118:119]
	global_load_dwordx4 v[142:145], v[126:127], off
	global_load_dwordx4 v[138:141], v[126:127], off offset:256
	s_nop 0
	global_load_dwordx4 v[126:129], v[118:119], off
	s_nop 0
	global_load_dwordx4 v[118:121], v[118:119], off offset:256
	s_cmp_gt_u32 s80, 63
	s_cbranch_scc1 .LBB0_632
	s_memrealtime s[30:31]
	s_branch .LBB0_619

.LBB0_692:
	s_lshl_b32 s5, s19, 5
	s_lshl_b32 s8, s18, 8
	v_lshrrev_b32_e32 v0, 1, v239
	s_add_i32 s4, s92, 64
	s_or_b32 s5, s8, s5
	v_and_or_b32 v220, v0, 24, s5
	s_lshl_b32 s35, s4, 8
	v_add_u32_e32 v118, s35, v240
	v_ashrrev_i32_e32 v221, 31, v220
	v_lshl_add_u64 v[120:121], v[220:221], 1, s[6:7]
	s_mov_b64 s[6:7], 0x4000000
	v_ashrrev_i32_e32 v119, 31, v118
	v_lshl_add_u64 v[120:121], v[120:121], 0, s[6:7]
	v_lshlrev_b64 v[224:225], 11, v[118:119]
	v_lshl_add_u64 v[126:127], v[120:121], 0, v[224:225]
	s_barrier
	v_and_b32_e32 v167, 64, v231
	v_xor_b32_e32 v0, 16, v231
	v_add_u32_e32 v167, 64, v167
	v_cmp_lt_i32_e32 vcc, v0, v167
	v_mul_f32_e32 v168, v137, v137
	v_fmac_f32_e32 v168, v136, v136
	v_cndmask_b32_e32 v0, v231, v0, vcc
	v_lshlrev_b32_e32 v241, 2, v0
	v_mul_f32_e32 v0, v135, v135
	v_fmac_f32_e32 v0, v134, v134
	v_add_f32_e32 v0, v0, v168
	v_mul_f32_e32 v168, v131, v131
	v_mul_f32_e32 v169, v133, v133
	v_fmac_f32_e32 v168, v130, v130
	v_fmac_f32_e32 v169, v132, v132
	v_add_f32_e32 v168, v168, v169
	v_add_f32_e32 v0, v168, v0
	v_mul_f32_e32 v168, v123, v123
	v_mul_f32_e32 v169, v125, v125
	v_fmac_f32_e32 v168, v122, v122
	v_fmac_f32_e32 v169, v124, v124
	v_add_f32_e32 v168, v168, v169
	v_add_f32_e32 v0, v168, v0
	v_mul_f32_e32 v168, v115, v115
	v_mul_f32_e32 v169, v117, v117
	v_fmac_f32_e32 v168, v114, v114
	v_fmac_f32_e32 v169, v116, v116
	v_add_f32_e32 v168, v168, v169
	v_add_f32_e32 v0, v168, v0
	ds_bpermute_b32 v168, v241, v0
	v_xor_b32_e32 v169, 32, v231
	v_cmp_lt_i32_e32 vcc, v169, v167
	s_lshl_b32 s5, s19, 2
	s_add_i32 s34, s5, 0
	v_cndmask_b32_e32 v167, v231, v169, vcc
	v_lshlrev_b32_e32 v242, 2, v167
	s_waitcnt lgkmcnt(0)
	v_add_f32_e32 v167, v0, v168
	ds_bpermute_b32 v168, v242, v167
	v_and_b32_e32 v0, 63, v239
	v_cmp_gt_u32_e64 s[40:41], 16, v0
	s_and_saveexec_b64 s[6:7], s[40:41]
	s_load_dwordx2 s[90:91], s[0:1], 0xb0
	v_readlane_b32 s64, v252, 3
	v_readlane_b32 s65, v255, 10
	v_readlane_b32 s68, v255, 11
	s_cbranch_execz .LBB0_694
	s_lshl_b32 s5, s76, 10
	s_add_i32 s5, s34, s5
	s_waitcnt lgkmcnt(0)
	v_add_f32_e32 v167, v167, v168
	v_lshl_add_u32 v168, v166, 4, s5
	ds_write_b32 v168, v167

.LBB0_713:
	s_or_b64 exec, exec, s[8:9]
	global_load_dwordx4 v[206:209], v[126:127], off
	global_load_dwordx4 v[202:205], v[126:127], off offset:256
	v_or_b32_e32 v126, 16, v118
	v_ashrrev_i32_e32 v127, 31, v126
	v_lshlrev_b64 v[126:127], 11, v[126:127]
	v_lshl_add_u64 v[126:127], v[120:121], 0, v[126:127]
	global_load_dwordx4 v[198:201], v[126:127], off
	global_load_dwordx4 v[194:197], v[126:127], off offset:256
	v_or_b32_e32 v126, 32, v118
	v_ashrrev_i32_e32 v127, 31, v126
	v_lshlrev_b64 v[126:127], 11, v[126:127]
	v_lshl_add_u64 v[126:127], v[120:121], 0, v[126:127]
	global_load_dwordx4 v[190:193], v[126:127], off
	global_load_dwordx4 v[186:189], v[126:127], off offset:256
	v_or_b32_e32 v126, 48, v118
	v_ashrrev_i32_e32 v127, 31, v126
	v_lshlrev_b64 v[126:127], 11, v[126:127]
	v_lshl_add_u64 v[126:127], v[120:121], 0, v[126:127]
	global_load_dwordx4 v[174:177], v[126:127], off
	global_load_dwordx4 v[162:165], v[126:127], off offset:256
	v_add_u32_e32 v126, 0x80, v118
	v_ashrrev_i32_e32 v127, 31, v126
	v_lshlrev_b64 v[126:127], 11, v[126:127]
	v_lshl_add_u64 v[126:127], v[120:121], 0, v[126:127]
	global_load_dwordx4 v[158:161], v[126:127], off
	global_load_dwordx4 v[154:157], v[126:127], off offset:256
	v_add_u32_e32 v126, 0x90, v118
	v_ashrrev_i32_e32 v127, 31, v126
	v_lshlrev_b64 v[126:127], 11, v[126:127]
	v_lshl_add_u64 v[126:127], v[120:121], 0, v[126:127]
	global_load_dwordx4 v[150:153], v[126:127], off
	global_load_dwordx4 v[146:149], v[126:127], off offset:256
	v_add_u32_e32 v126, 0xa0, v118
	v_add_u32_e32 v118, 0xb0, v118
	v_ashrrev_i32_e32 v127, 31, v126
	v_ashrrev_i32_e32 v119, 31, v118
	v_lshlrev_b64 v[126:127], 11, v[126:127]
	v_lshlrev_b64 v[118:119], 11, v[118:119]
	v_lshl_add_u64 v[126:127], v[120:121], 0, v[126:127]
	v_lshl_add_u64 v[118:119], v[120:121], 0, v[118:119]
	global_load_dwordx4 v[142:145], v[126:127], off
	global_load_dwordx4 v[138:141], v[126:127], off offset:256
	s_nop 0
	global_load_dwordx4 v[126:129], v[118:119], off
	s_nop 0
	global_load_dwordx4 v[118:121], v[118:119], off offset:256
	s_cmp_gt_u32 s70, 63
	s_cbranch_scc1 .LBB0_730
	s_memrealtime s[28:29]
	s_branch .LBB0_717

.LBB0_1533:
	s_lshl_b32 s4, s49, 5
	s_lshl_b32 s8, s16, 8
	v_lshrrev_b32_e32 v0, 1, v166
	s_or_b32 s4, s8, s4
	v_and_or_b32 v220, v0, 24, s4
	s_lshl_b32 s29, s47, 8
	v_add_u32_e32 v118, s29, v240
	v_ashrrev_i32_e32 v221, 31, v220
	v_lshl_add_u64 v[120:121], v[220:221], 1, s[6:7]
	s_mov_b64 s[6:7], 0x4000000
	v_ashrrev_i32_e32 v119, 31, v118
	v_lshl_add_u64 v[120:121], v[120:121], 0, s[6:7]
	v_lshlrev_b64 v[224:225], 11, v[118:119]
	v_lshl_add_u64 v[126:127], v[120:121], 0, v[224:225]
	s_barrier
	v_and_b32_e32 v168, 64, v231
	v_xor_b32_e32 v0, 16, v231
	v_add_u32_e32 v168, 64, v168
	v_cmp_lt_i32_e32 vcc, v0, v168
	v_mul_f32_e32 v169, v137, v137
	v_fmac_f32_e32 v169, v136, v136
	v_cndmask_b32_e32 v0, v231, v0, vcc
	v_lshlrev_b32_e32 v241, 2, v0
	v_mul_f32_e32 v0, v135, v135
	v_fmac_f32_e32 v0, v134, v134
	v_add_f32_e32 v0, v0, v169
	v_mul_f32_e32 v169, v131, v131
	v_mul_f32_e32 v170, v133, v133
	v_fmac_f32_e32 v169, v130, v130
	v_fmac_f32_e32 v170, v132, v132
	v_add_f32_e32 v169, v169, v170
	v_add_f32_e32 v0, v169, v0
	v_mul_f32_e32 v169, v123, v123
	v_mul_f32_e32 v170, v125, v125
	v_fmac_f32_e32 v169, v122, v122
	v_fmac_f32_e32 v170, v124, v124
	v_add_f32_e32 v169, v169, v170
	v_add_f32_e32 v0, v169, v0
	v_mul_f32_e32 v169, v115, v115
	v_mul_f32_e32 v170, v117, v117
	v_fmac_f32_e32 v169, v114, v114
	v_fmac_f32_e32 v170, v116, v116
	v_add_f32_e32 v169, v169, v170
	v_add_f32_e32 v0, v169, v0
	ds_bpermute_b32 v169, v241, v0
	v_xor_b32_e32 v170, 32, v231
	v_cmp_lt_i32_e32 vcc, v170, v168
	s_lshl_b32 s4, s49, 2
	s_add_i32 s28, s4, 0
	v_cndmask_b32_e32 v168, v231, v170, vcc
	v_lshlrev_b32_e32 v242, 2, v168
	s_waitcnt lgkmcnt(0)
	v_add_f32_e32 v168, v0, v169
	ds_bpermute_b32 v169, v242, v168
	v_and_b32_e32 v0, 63, v166
	v_cmp_gt_u32_e64 s[40:41], 16, v0
	s_and_saveexec_b64 s[6:7], s[40:41]
	v_readlane_b32 s64, v252, 3
	v_readlane_b32 s65, v255, 10
	v_readlane_b32 s68, v255, 11
	s_cbranch_execz .LBB0_1535
	s_lshl_b32 s4, s46, 10
	s_add_i32 s4, s28, s4
	s_waitcnt lgkmcnt(0)
	v_add_f32_e32 v168, v168, v169
	v_lshl_add_u32 v169, v167, 4, s4
	ds_write_b32 v169, v168

.LBB0_1554:
	s_or_b64 exec, exec, s[8:9]
	global_load_dwordx4 v[206:209], v[126:127], off
	global_load_dwordx4 v[202:205], v[126:127], off offset:256
	v_or_b32_e32 v126, 16, v118
	v_ashrrev_i32_e32 v127, 31, v126
	v_lshlrev_b64 v[126:127], 11, v[126:127]
	v_lshl_add_u64 v[126:127], v[120:121], 0, v[126:127]
	global_load_dwordx4 v[198:201], v[126:127], off
	global_load_dwordx4 v[194:197], v[126:127], off offset:256
	v_or_b32_e32 v126, 32, v118
	v_ashrrev_i32_e32 v127, 31, v126
	v_lshlrev_b64 v[126:127], 11, v[126:127]
	v_lshl_add_u64 v[126:127], v[120:121], 0, v[126:127]
	global_load_dwordx4 v[190:193], v[126:127], off
	global_load_dwordx4 v[186:189], v[126:127], off offset:256
	v_or_b32_e32 v126, 48, v118
	v_ashrrev_i32_e32 v127, 31, v126
	v_lshlrev_b64 v[126:127], 11, v[126:127]
	v_lshl_add_u64 v[126:127], v[120:121], 0, v[126:127]
	global_load_dwordx4 v[174:177], v[126:127], off
	global_load_dwordx4 v[162:165], v[126:127], off offset:256
	v_add_u32_e32 v126, 0x80, v118
	v_ashrrev_i32_e32 v127, 31, v126
	v_lshlrev_b64 v[126:127], 11, v[126:127]
	v_lshl_add_u64 v[126:127], v[120:121], 0, v[126:127]
	global_load_dwordx4 v[158:161], v[126:127], off
	global_load_dwordx4 v[154:157], v[126:127], off offset:256
	v_add_u32_e32 v126, 0x90, v118
	v_ashrrev_i32_e32 v127, 31, v126
	v_lshlrev_b64 v[126:127], 11, v[126:127]
	v_lshl_add_u64 v[126:127], v[120:121], 0, v[126:127]
	global_load_dwordx4 v[150:153], v[126:127], off
	global_load_dwordx4 v[146:149], v[126:127], off offset:256
	v_add_u32_e32 v126, 0xa0, v118
	v_add_u32_e32 v118, 0xb0, v118
	v_ashrrev_i32_e32 v127, 31, v126
	v_ashrrev_i32_e32 v119, 31, v118
	v_lshlrev_b64 v[126:127], 11, v[126:127]
	v_lshlrev_b64 v[118:119], 11, v[118:119]
	v_lshl_add_u64 v[126:127], v[120:121], 0, v[126:127]
	v_lshl_add_u64 v[118:119], v[120:121], 0, v[118:119]
	global_load_dwordx4 v[142:145], v[126:127], off
	global_load_dwordx4 v[138:141], v[126:127], off offset:256
	s_nop 0
	global_load_dwordx4 v[126:129], v[118:119], off
	s_nop 0
	global_load_dwordx4 v[118:121], v[118:119], off offset:256
	s_cmp_gt_u32 s48, 63
	s_cbranch_scc1 .LBB0_1571
	s_memrealtime s[24:25]
	s_branch .LBB0_1558

.LBB0_1630:
	s_lshl_b32 s8, s45, 5
	s_lshl_b32 s9, s16, 8
	v_lshrrev_b32_e32 v0, 1, v239
	s_add_i32 s4, s76, 64
	s_or_b32 s8, s9, s8
	v_and_or_b32 v220, v0, 24, s8
	s_lshl_b32 s29, s4, 8
	v_add_u32_e32 v118, s29, v240
	v_ashrrev_i32_e32 v221, 31, v220
	v_lshl_add_u64 v[120:121], v[220:221], 1, s[6:7]
	s_mov_b64 s[6:7], 0x4000000
	v_ashrrev_i32_e32 v119, 31, v118
	v_lshl_add_u64 v[120:121], v[120:121], 0, s[6:7]
	v_lshlrev_b64 v[224:225], 11, v[118:119]
	v_lshl_add_u64 v[126:127], v[120:121], 0, v[224:225]
	s_barrier
	v_and_b32_e32 v167, 64, v231
	v_xor_b32_e32 v0, 16, v231
	v_add_u32_e32 v167, 64, v167
	v_cmp_lt_i32_e32 vcc, v0, v167
	v_mul_f32_e32 v168, v137, v137
	v_fmac_f32_e32 v168, v136, v136
	v_cndmask_b32_e32 v0, v231, v0, vcc
	v_lshlrev_b32_e32 v241, 2, v0
	v_mul_f32_e32 v0, v135, v135
	v_fmac_f32_e32 v0, v134, v134
	v_add_f32_e32 v0, v0, v168
	v_mul_f32_e32 v168, v131, v131
	v_mul_f32_e32 v169, v133, v133
	v_fmac_f32_e32 v168, v130, v130
	v_fmac_f32_e32 v169, v132, v132
	v_add_f32_e32 v168, v168, v169
	v_add_f32_e32 v0, v168, v0
	v_mul_f32_e32 v168, v123, v123
	v_mul_f32_e32 v169, v125, v125
	v_fmac_f32_e32 v168, v122, v122
	v_fmac_f32_e32 v169, v124, v124
	v_add_f32_e32 v168, v168, v169
	v_add_f32_e32 v0, v168, v0
	v_mul_f32_e32 v168, v115, v115
	v_mul_f32_e32 v169, v117, v117
	v_fmac_f32_e32 v168, v114, v114
	v_fmac_f32_e32 v169, v116, v116
	v_add_f32_e32 v168, v168, v169
	v_add_f32_e32 v0, v168, v0
	ds_bpermute_b32 v168, v241, v0
	v_xor_b32_e32 v169, 32, v231
	v_cmp_lt_i32_e32 vcc, v169, v167
	s_lshl_b32 s6, s45, 2
	s_add_i32 s28, s6, 0
	v_cndmask_b32_e32 v167, v231, v169, vcc
	v_lshlrev_b32_e32 v242, 2, v167
	s_waitcnt lgkmcnt(0)
	v_add_f32_e32 v167, v0, v168
	ds_bpermute_b32 v168, v242, v167
	v_and_b32_e32 v0, 63, v239
	v_cmp_gt_u32_e64 s[38:39], 16, v0
	s_and_saveexec_b64 s[6:7], s[38:39]
	v_readlane_b32 s64, v252, 3
	v_readlane_b32 s65, v255, 10
	v_readlane_b32 s68, v255, 11
	s_cbranch_execz .LBB0_1632
	s_lshl_b32 s8, s44, 10
	s_add_i32 s8, s28, s8
	s_waitcnt lgkmcnt(0)
	v_add_f32_e32 v167, v167, v168
	v_lshl_add_u32 v168, v166, 4, s8
	ds_write_b32 v168, v167

.LBB0_1651:
	s_or_b64 exec, exec, s[8:9]
	global_load_dwordx4 v[206:209], v[126:127], off
	global_load_dwordx4 v[202:205], v[126:127], off offset:256
	v_or_b32_e32 v126, 16, v118
	v_ashrrev_i32_e32 v127, 31, v126
	v_lshlrev_b64 v[126:127], 11, v[126:127]
	v_lshl_add_u64 v[126:127], v[120:121], 0, v[126:127]
	global_load_dwordx4 v[198:201], v[126:127], off
	global_load_dwordx4 v[194:197], v[126:127], off offset:256
	v_or_b32_e32 v126, 32, v118
	v_ashrrev_i32_e32 v127, 31, v126
	v_lshlrev_b64 v[126:127], 11, v[126:127]
	v_lshl_add_u64 v[126:127], v[120:121], 0, v[126:127]
	global_load_dwordx4 v[190:193], v[126:127], off
	global_load_dwordx4 v[186:189], v[126:127], off offset:256
	v_or_b32_e32 v126, 48, v118
	v_ashrrev_i32_e32 v127, 31, v126
	v_lshlrev_b64 v[126:127], 11, v[126:127]
	v_lshl_add_u64 v[126:127], v[120:121], 0, v[126:127]
	global_load_dwordx4 v[174:177], v[126:127], off
	global_load_dwordx4 v[162:165], v[126:127], off offset:256
	v_add_u32_e32 v126, 0x80, v118
	v_ashrrev_i32_e32 v127, 31, v126
	v_lshlrev_b64 v[126:127], 11, v[126:127]
	v_lshl_add_u64 v[126:127], v[120:121], 0, v[126:127]
	global_load_dwordx4 v[158:161], v[126:127], off
	global_load_dwordx4 v[154:157], v[126:127], off offset:256
	v_add_u32_e32 v126, 0x90, v118
	v_ashrrev_i32_e32 v127, 31, v126
	v_lshlrev_b64 v[126:127], 11, v[126:127]
	v_lshl_add_u64 v[126:127], v[120:121], 0, v[126:127]
	global_load_dwordx4 v[150:153], v[126:127], off
	global_load_dwordx4 v[146:149], v[126:127], off offset:256
	v_add_u32_e32 v126, 0xa0, v118
	v_add_u32_e32 v118, 0xb0, v118
	v_ashrrev_i32_e32 v127, 31, v126
	v_ashrrev_i32_e32 v119, 31, v118
	v_lshlrev_b64 v[126:127], 11, v[126:127]
	v_lshlrev_b64 v[118:119], 11, v[118:119]
	v_lshl_add_u64 v[126:127], v[120:121], 0, v[126:127]
	v_lshl_add_u64 v[118:119], v[120:121], 0, v[118:119]
	global_load_dwordx4 v[142:145], v[126:127], off
	global_load_dwordx4 v[138:141], v[126:127], off offset:256
	s_nop 0
	global_load_dwordx4 v[126:129], v[118:119], off
	s_nop 0
	global_load_dwordx4 v[118:121], v[118:119], off offset:256
	s_cmp_gt_u32 s46, 63
	s_cbranch_scc1 .LBB0_1668
	s_memrealtime s[24:25]
	s_branch .LBB0_1655

.LBB0_2375:
	s_lshl_b32 s4, s17, 5
	s_add_u32 s6, s6, s28
	s_addc_u32 s7, s7, s29
	s_lshl_b32 s8, s16, 8
	v_lshrrev_b32_e32 v122, 1, v0
	s_or_b32 s4, s8, s4
	s_lshl_b32 s35, s94, 8
	v_and_or_b32 v220, v122, 24, s4
	v_add_u32_e32 v122, s35, v240
	v_ashrrev_i32_e32 v221, 31, v220
	v_ashrrev_i32_e32 v123, 31, v122
	v_lshl_add_u64 v[124:125], v[220:221], 1, s[6:7]
	v_lshlrev_b64 v[224:225], 11, v[122:123]
	v_lshl_add_u64 v[126:127], v[124:125], 0, v[224:225]
	s_barrier
	v_and_b32_e32 v168, 64, v231
	v_xor_b32_e32 v167, 16, v231
	v_add_u32_e32 v168, 64, v168
	v_cmp_lt_i32_e32 vcc, v167, v168
	v_mul_f32_e32 v169, v137, v137
	v_fmac_f32_e32 v169, v136, v136
	v_cndmask_b32_e32 v167, v231, v167, vcc
	v_lshlrev_b32_e32 v241, 2, v167
	v_mul_f32_e32 v167, v135, v135
	v_fmac_f32_e32 v167, v134, v134
	v_add_f32_e32 v167, v167, v169
	v_mul_f32_e32 v169, v131, v131
	v_mul_f32_e32 v170, v133, v133
	v_fmac_f32_e32 v169, v130, v130
	v_fmac_f32_e32 v170, v132, v132
	v_add_f32_e32 v169, v169, v170
	v_add_f32_e32 v167, v169, v167
	v_mul_f32_e32 v169, v119, v119
	v_mul_f32_e32 v170, v121, v121
	v_fmac_f32_e32 v169, v118, v118
	v_fmac_f32_e32 v170, v120, v120
	v_add_f32_e32 v169, v169, v170
	v_add_f32_e32 v167, v169, v167
	v_mul_f32_e32 v169, v115, v115
	v_mul_f32_e32 v170, v117, v117
	v_fmac_f32_e32 v169, v114, v114
	v_fmac_f32_e32 v170, v116, v116
	v_add_f32_e32 v169, v169, v170
	v_add_f32_e32 v167, v169, v167
	ds_bpermute_b32 v169, v241, v167
	v_xor_b32_e32 v170, 32, v231
	v_cmp_lt_i32_e32 vcc, v170, v168
	s_lshl_b32 s4, s17, 2
	s_add_i32 s34, s4, 0
	v_cndmask_b32_e32 v168, v231, v170, vcc
	v_lshlrev_b32_e32 v242, 2, v168
	s_waitcnt lgkmcnt(0)
	v_add_f32_e32 v168, v167, v169
	ds_bpermute_b32 v169, v242, v168
	v_and_b32_e32 v167, 63, v0
	v_cmp_gt_u32_e64 s[40:41], 16, v167
	s_and_saveexec_b64 s[6:7], s[40:41]
	s_load_dwordx2 s[90:91], s[0:1], 0xb0
	v_readlane_b32 s36, v255, 32
	v_readlane_b32 s64, v252, 3
	v_readlane_b32 s65, v255, 10
	v_readlane_b32 s68, v255, 11
	v_readlane_b32 s74, v255, 12
	v_readlane_b32 s95, v255, 13
	s_movk_i32 s92, 0x2b20
	v_readlane_b32 s33, v255, 22
	v_readlane_b32 s37, v255, 33
	s_cbranch_execz .LBB0_2377
	s_lshl_b32 s4, s93, 10
	s_add_i32 s4, s34, s4
	s_waitcnt lgkmcnt(0)
	v_add_f32_e32 v168, v168, v169
	v_lshl_add_u32 v169, v166, 4, s4
	ds_write_b32 v169, v168

.LBB0_2396:
	s_or_b64 exec, exec, s[26:27]
	global_load_dwordx4 v[206:209], v[126:127], off
	global_load_dwordx4 v[202:205], v[126:127], off offset:256
	v_or_b32_e32 v126, 16, v122
	v_ashrrev_i32_e32 v127, 31, v126
	v_lshlrev_b64 v[126:127], 11, v[126:127]
	v_lshl_add_u64 v[126:127], v[124:125], 0, v[126:127]
	global_load_dwordx4 v[198:201], v[126:127], off
	global_load_dwordx4 v[194:197], v[126:127], off offset:256
	v_or_b32_e32 v126, 32, v122
	v_ashrrev_i32_e32 v127, 31, v126
	v_lshlrev_b64 v[126:127], 11, v[126:127]
	v_lshl_add_u64 v[126:127], v[124:125], 0, v[126:127]
	global_load_dwordx4 v[190:193], v[126:127], off
	global_load_dwordx4 v[186:189], v[126:127], off offset:256
	v_or_b32_e32 v126, 48, v122
	v_ashrrev_i32_e32 v127, 31, v126
	v_lshlrev_b64 v[126:127], 11, v[126:127]
	v_lshl_add_u64 v[126:127], v[124:125], 0, v[126:127]
	global_load_dwordx4 v[174:177], v[126:127], off
	global_load_dwordx4 v[162:165], v[126:127], off offset:256
	v_add_u32_e32 v126, 0x80, v122
	v_ashrrev_i32_e32 v127, 31, v126
	v_lshlrev_b64 v[126:127], 11, v[126:127]
	v_lshl_add_u64 v[126:127], v[124:125], 0, v[126:127]
	global_load_dwordx4 v[158:161], v[126:127], off
	global_load_dwordx4 v[154:157], v[126:127], off offset:256
	v_add_u32_e32 v126, 0x90, v122
	v_ashrrev_i32_e32 v127, 31, v126
	v_lshlrev_b64 v[126:127], 11, v[126:127]
	v_lshl_add_u64 v[126:127], v[124:125], 0, v[126:127]
	global_load_dwordx4 v[150:153], v[126:127], off
	global_load_dwordx4 v[146:149], v[126:127], off offset:256
	v_add_u32_e32 v126, 0xa0, v122
	v_add_u32_e32 v122, 0xb0, v122
	v_ashrrev_i32_e32 v127, 31, v126
	v_ashrrev_i32_e32 v123, 31, v122
	v_lshlrev_b64 v[126:127], 11, v[126:127]
	v_lshlrev_b64 v[122:123], 11, v[122:123]
	v_lshl_add_u64 v[126:127], v[124:125], 0, v[126:127]
	v_lshl_add_u64 v[122:123], v[124:125], 0, v[122:123]
	global_load_dwordx4 v[142:145], v[126:127], off
	global_load_dwordx4 v[138:141], v[126:127], off offset:256
	s_nop 0
	global_load_dwordx4 v[126:129], v[122:123], off
	s_nop 0
	global_load_dwordx4 v[122:125], v[122:123], off offset:256
	s_cmp_gt_u32 s83, 63
	s_cbranch_scc1 .LBB0_2413
	s_memrealtime s[26:27]
	s_branch .LBB0_2400

.LBB0_2475:
	s_lshl_b32 s8, s15, 5
	s_add_u32 s6, s6, s26
	s_addc_u32 s7, s7, s27
	s_add_i32 s4, s95, 64
	s_lshl_b32 s9, s14, 8
	v_lshrrev_b32_e32 v122, 1, v239
	s_or_b32 s8, s9, s8
	s_lshl_b32 s31, s4, 8
	v_and_or_b32 v220, v122, 24, s8
	v_add_u32_e32 v122, s31, v240
	v_ashrrev_i32_e32 v221, 31, v220
	v_ashrrev_i32_e32 v123, 31, v122
	v_lshl_add_u64 v[124:125], v[220:221], 1, s[6:7]
	v_lshlrev_b64 v[224:225], 11, v[122:123]
	v_lshl_add_u64 v[126:127], v[124:125], 0, v[224:225]
	s_barrier
	v_and_b32_e32 v167, 64, v231
	v_xor_b32_e32 v166, 16, v231
	v_add_u32_e32 v167, 64, v167
	v_cmp_lt_i32_e32 vcc, v166, v167
	v_mul_f32_e32 v168, v137, v137
	v_fmac_f32_e32 v168, v136, v136
	v_cndmask_b32_e32 v166, v231, v166, vcc
	v_lshlrev_b32_e32 v241, 2, v166
	v_mul_f32_e32 v166, v135, v135
	v_fmac_f32_e32 v166, v134, v134
	v_add_f32_e32 v166, v166, v168
	v_mul_f32_e32 v168, v131, v131
	v_mul_f32_e32 v169, v133, v133
	v_fmac_f32_e32 v168, v130, v130
	v_fmac_f32_e32 v169, v132, v132
	v_add_f32_e32 v168, v168, v169
	v_add_f32_e32 v166, v168, v166
	v_mul_f32_e32 v168, v119, v119
	v_mul_f32_e32 v169, v121, v121
	v_fmac_f32_e32 v168, v118, v118
	v_fmac_f32_e32 v169, v120, v120
	v_add_f32_e32 v168, v168, v169
	v_add_f32_e32 v166, v168, v166
	v_mul_f32_e32 v168, v115, v115
	v_mul_f32_e32 v169, v117, v117
	v_fmac_f32_e32 v168, v114, v114
	v_fmac_f32_e32 v169, v116, v116
	v_add_f32_e32 v168, v168, v169
	v_add_f32_e32 v166, v168, v166
	ds_bpermute_b32 v168, v241, v166
	v_xor_b32_e32 v169, 32, v231
	v_cmp_lt_i32_e32 vcc, v169, v167
	s_lshl_b32 s6, s15, 2
	s_add_i32 s30, s6, 0
	v_cndmask_b32_e32 v167, v231, v169, vcc
	v_lshlrev_b32_e32 v242, 2, v167
	s_waitcnt lgkmcnt(0)
	v_add_f32_e32 v167, v166, v168
	ds_bpermute_b32 v168, v242, v167
	v_and_b32_e32 v166, 63, v239
	v_cmp_gt_u32_e64 s[38:39], 16, v166
	s_and_saveexec_b64 s[6:7], s[38:39]
	s_load_dwordx2 s[90:91], s[0:1], 0xb0
	v_readlane_b32 s64, v252, 3
	v_readlane_b32 s65, v255, 10
	v_readlane_b32 s68, v255, 11
	s_movk_i32 s92, 0x2b20
	s_cbranch_execz .LBB0_2477
	s_lshl_b32 s8, s80, 10
	s_add_i32 s8, s30, s8
	s_waitcnt lgkmcnt(0)
	v_add_f32_e32 v167, v167, v168
	v_lshl_add_u32 v168, v0, 4, s8
	ds_write_b32 v168, v167

.LBB0_2496:
	s_or_b64 exec, exec, s[24:25]
	global_load_dwordx4 v[206:209], v[126:127], off
	global_load_dwordx4 v[202:205], v[126:127], off offset:256
	v_or_b32_e32 v126, 16, v122
	v_ashrrev_i32_e32 v127, 31, v126
	v_lshlrev_b64 v[126:127], 11, v[126:127]
	v_lshl_add_u64 v[126:127], v[124:125], 0, v[126:127]
	global_load_dwordx4 v[198:201], v[126:127], off
	global_load_dwordx4 v[194:197], v[126:127], off offset:256
	v_or_b32_e32 v126, 32, v122
	v_ashrrev_i32_e32 v127, 31, v126
	v_lshlrev_b64 v[126:127], 11, v[126:127]
	v_lshl_add_u64 v[126:127], v[124:125], 0, v[126:127]
	global_load_dwordx4 v[190:193], v[126:127], off
	global_load_dwordx4 v[186:189], v[126:127], off offset:256
	v_or_b32_e32 v126, 48, v122
	v_ashrrev_i32_e32 v127, 31, v126
	v_lshlrev_b64 v[126:127], 11, v[126:127]
	v_lshl_add_u64 v[126:127], v[124:125], 0, v[126:127]
	global_load_dwordx4 v[174:177], v[126:127], off
	global_load_dwordx4 v[162:165], v[126:127], off offset:256
	v_add_u32_e32 v126, 0x80, v122
	v_ashrrev_i32_e32 v127, 31, v126
	v_lshlrev_b64 v[126:127], 11, v[126:127]
	v_lshl_add_u64 v[126:127], v[124:125], 0, v[126:127]
	global_load_dwordx4 v[158:161], v[126:127], off
	global_load_dwordx4 v[154:157], v[126:127], off offset:256
	v_add_u32_e32 v126, 0x90, v122
	v_ashrrev_i32_e32 v127, 31, v126
	v_lshlrev_b64 v[126:127], 11, v[126:127]
	v_lshl_add_u64 v[126:127], v[124:125], 0, v[126:127]
	global_load_dwordx4 v[150:153], v[126:127], off
	global_load_dwordx4 v[146:149], v[126:127], off offset:256
	v_add_u32_e32 v126, 0xa0, v122
	v_add_u32_e32 v122, 0xb0, v122
	v_ashrrev_i32_e32 v127, 31, v126
	v_ashrrev_i32_e32 v123, 31, v122
	v_lshlrev_b64 v[126:127], 11, v[126:127]
	v_lshlrev_b64 v[122:123], 11, v[122:123]
	v_lshl_add_u64 v[126:127], v[124:125], 0, v[126:127]
	v_lshl_add_u64 v[122:123], v[124:125], 0, v[122:123]
	global_load_dwordx4 v[142:145], v[126:127], off
	global_load_dwordx4 v[138:141], v[126:127], off offset:256
	s_nop 0
	global_load_dwordx4 v[126:129], v[122:123], off
	s_nop 0
	global_load_dwordx4 v[122:125], v[122:123], off offset:256
	s_cmp_gt_u32 s78, 63
	s_cbranch_scc1 .LBB0_2513
	s_memrealtime s[24:25]
	s_branch .LBB0_2500

.LBB0_2710:
	s_lshl_b32 s4, s62, 5
	s_lshl_b32 s24, s12, 8
	v_lshrrev_b32_e32 v118, 1, v0
	s_or_b32 s4, s24, s4
	v_and_or_b32 v220, v118, 24, s4
	s_lshl_b32 s29, s53, 8
	v_add_u32_e32 v118, s29, v240
	v_ashrrev_i32_e32 v221, 31, v220
	v_lshl_add_u64 v[120:121], v[220:221], 1, s[22:23]
	s_mov_b64 s[22:23], 0x4000000
	v_ashrrev_i32_e32 v119, 31, v118
	v_lshl_add_u64 v[120:121], v[120:121], 0, s[22:23]
	v_lshlrev_b64 v[224:225], 11, v[118:119]
	v_lshl_add_u64 v[126:127], v[120:121], 0, v[224:225]
	s_barrier
	v_and_b32_e32 v168, 64, v231
	v_xor_b32_e32 v167, 16, v231
	v_add_u32_e32 v168, 64, v168
	v_cmp_lt_i32_e32 vcc, v167, v168
	v_mul_f32_e32 v169, v137, v137
	v_fmac_f32_e32 v169, v136, v136
	v_cndmask_b32_e32 v167, v231, v167, vcc
	v_lshlrev_b32_e32 v241, 2, v167
	v_mul_f32_e32 v167, v135, v135
	v_fmac_f32_e32 v167, v134, v134
	v_add_f32_e32 v167, v167, v169
	v_mul_f32_e32 v169, v131, v131
	v_mul_f32_e32 v170, v133, v133
	v_fmac_f32_e32 v169, v130, v130
	v_fmac_f32_e32 v170, v132, v132
	v_add_f32_e32 v169, v169, v170
	v_add_f32_e32 v167, v169, v167
	v_mul_f32_e32 v169, v123, v123
	v_mul_f32_e32 v170, v125, v125
	v_fmac_f32_e32 v169, v122, v122
	v_fmac_f32_e32 v170, v124, v124
	v_add_f32_e32 v169, v169, v170
	v_add_f32_e32 v167, v169, v167
	v_mul_f32_e32 v169, v115, v115
	v_mul_f32_e32 v170, v117, v117
	v_fmac_f32_e32 v169, v114, v114
	v_fmac_f32_e32 v170, v116, v116
	v_add_f32_e32 v169, v169, v170
	v_add_f32_e32 v167, v169, v167
	ds_bpermute_b32 v169, v241, v167
	v_xor_b32_e32 v170, 32, v231
	v_cmp_lt_i32_e32 vcc, v170, v168
	s_lshl_b32 s4, s62, 2
	s_add_i32 s28, s4, 0
	v_cndmask_b32_e32 v168, v231, v170, vcc
	v_lshlrev_b32_e32 v242, 2, v168
	s_waitcnt lgkmcnt(0)
	v_add_f32_e32 v168, v167, v169
	ds_bpermute_b32 v169, v242, v168
	v_and_b32_e32 v167, 63, v0
	v_cmp_gt_u32_e64 s[40:41], 16, v167
	s_and_saveexec_b64 s[22:23], s[40:41]
	v_readlane_b32 s64, v252, 3
	v_readlane_b32 s65, v255, 10
	v_readlane_b32 s68, v255, 11
	v_readlane_b32 s70, v255, 14
	v_readlane_b32 s71, v255, 15
	s_cbranch_execz .LBB0_2712
	s_lshl_b32 s4, s52, 10
	s_add_i32 s4, s28, s4
	s_waitcnt lgkmcnt(0)
	v_add_f32_e32 v168, v168, v169
	v_lshl_add_u32 v169, v166, 4, s4
	ds_write_b32 v169, v168

.LBB0_2731:
	s_or_b64 exec, exec, s[22:23]
	global_load_dwordx4 v[206:209], v[126:127], off
	global_load_dwordx4 v[202:205], v[126:127], off offset:256
	v_or_b32_e32 v126, 16, v118
	v_ashrrev_i32_e32 v127, 31, v126
	v_lshlrev_b64 v[126:127], 11, v[126:127]
	v_lshl_add_u64 v[126:127], v[120:121], 0, v[126:127]
	global_load_dwordx4 v[198:201], v[126:127], off
	global_load_dwordx4 v[194:197], v[126:127], off offset:256
	v_or_b32_e32 v126, 32, v118
	v_ashrrev_i32_e32 v127, 31, v126
	v_lshlrev_b64 v[126:127], 11, v[126:127]
	v_lshl_add_u64 v[126:127], v[120:121], 0, v[126:127]
	global_load_dwordx4 v[190:193], v[126:127], off
	global_load_dwordx4 v[186:189], v[126:127], off offset:256
	v_or_b32_e32 v126, 48, v118
	v_ashrrev_i32_e32 v127, 31, v126
	v_lshlrev_b64 v[126:127], 11, v[126:127]
	v_lshl_add_u64 v[126:127], v[120:121], 0, v[126:127]
	global_load_dwordx4 v[174:177], v[126:127], off
	global_load_dwordx4 v[162:165], v[126:127], off offset:256
	v_add_u32_e32 v126, 0x80, v118
	v_ashrrev_i32_e32 v127, 31, v126
	v_lshlrev_b64 v[126:127], 11, v[126:127]
	v_lshl_add_u64 v[126:127], v[120:121], 0, v[126:127]
	global_load_dwordx4 v[158:161], v[126:127], off
	global_load_dwordx4 v[154:157], v[126:127], off offset:256
	v_add_u32_e32 v126, 0x90, v118
	v_ashrrev_i32_e32 v127, 31, v126
	v_lshlrev_b64 v[126:127], 11, v[126:127]
	v_lshl_add_u64 v[126:127], v[120:121], 0, v[126:127]
	global_load_dwordx4 v[150:153], v[126:127], off
	global_load_dwordx4 v[146:149], v[126:127], off offset:256
	v_add_u32_e32 v126, 0xa0, v118
	v_add_u32_e32 v118, 0xb0, v118
	v_ashrrev_i32_e32 v127, 31, v126
	v_ashrrev_i32_e32 v119, 31, v118
	v_lshlrev_b64 v[126:127], 11, v[126:127]
	v_lshlrev_b64 v[118:119], 11, v[118:119]
	v_lshl_add_u64 v[126:127], v[120:121], 0, v[126:127]
	v_lshl_add_u64 v[118:119], v[120:121], 0, v[118:119]
	global_load_dwordx4 v[142:145], v[126:127], off
	global_load_dwordx4 v[138:141], v[126:127], off offset:256
	s_nop 0
	global_load_dwordx4 v[126:129], v[118:119], off
	s_nop 0
	global_load_dwordx4 v[118:121], v[118:119], off offset:256
	s_cmp_gt_u32 s49, 63
	s_cbranch_scc1 .LBB0_2748
	s_memrealtime s[22:23]
	s_branch .LBB0_2735

.LBB0_2803:
	s_lshl_b32 s24, s52, 5
	s_lshl_b32 s25, s12, 8
	v_lshrrev_b32_e32 v118, 1, v0
	s_add_i32 s4, s80, 64
	s_or_b32 s24, s25, s24
	v_and_or_b32 v220, v118, 24, s24
	s_lshl_b32 s29, s4, 8
	v_add_u32_e32 v118, s29, v240
	v_ashrrev_i32_e32 v221, 31, v220
	v_lshl_add_u64 v[120:121], v[220:221], 1, s[22:23]
	s_mov_b64 s[22:23], 0x4000000
	v_ashrrev_i32_e32 v119, 31, v118
	v_lshl_add_u64 v[120:121], v[120:121], 0, s[22:23]
	v_lshlrev_b64 v[224:225], 11, v[118:119]
	v_lshl_add_u64 v[126:127], v[120:121], 0, v[224:225]
	s_barrier
	v_and_b32_e32 v168, 64, v231
	v_xor_b32_e32 v167, 16, v231
	v_add_u32_e32 v168, 64, v168
	v_cmp_lt_i32_e32 vcc, v167, v168
	v_mul_f32_e32 v169, v137, v137
	v_fmac_f32_e32 v169, v136, v136
	v_cndmask_b32_e32 v167, v231, v167, vcc
	v_lshlrev_b32_e32 v241, 2, v167
	v_mul_f32_e32 v167, v135, v135
	v_fmac_f32_e32 v167, v134, v134
	v_add_f32_e32 v167, v167, v169
	v_mul_f32_e32 v169, v131, v131
	v_mul_f32_e32 v170, v133, v133
	v_fmac_f32_e32 v169, v130, v130
	v_fmac_f32_e32 v170, v132, v132
	v_add_f32_e32 v169, v169, v170
	v_add_f32_e32 v167, v169, v167
	v_mul_f32_e32 v169, v123, v123
	v_mul_f32_e32 v170, v125, v125
	v_fmac_f32_e32 v169, v122, v122
	v_fmac_f32_e32 v170, v124, v124
	v_add_f32_e32 v169, v169, v170
	v_add_f32_e32 v167, v169, v167
	v_mul_f32_e32 v169, v115, v115
	v_mul_f32_e32 v170, v117, v117
	v_fmac_f32_e32 v169, v114, v114
	v_fmac_f32_e32 v170, v116, v116
	v_add_f32_e32 v169, v169, v170
	v_add_f32_e32 v167, v169, v167
	ds_bpermute_b32 v169, v241, v167
	v_xor_b32_e32 v170, 32, v231
	v_cmp_lt_i32_e32 vcc, v170, v168
	s_lshl_b32 s22, s52, 2
	s_add_i32 s28, s22, 0
	v_cndmask_b32_e32 v168, v231, v170, vcc
	v_lshlrev_b32_e32 v242, 2, v168
	s_waitcnt lgkmcnt(0)
	v_add_f32_e32 v168, v167, v169
	ds_bpermute_b32 v169, v242, v168
	v_and_b32_e32 v167, 63, v0
	v_cmp_gt_u32_e64 s[40:41], 16, v167
	s_and_saveexec_b64 s[22:23], s[40:41]
	v_readlane_b32 s64, v252, 3
	v_readlane_b32 s65, v255, 10
	v_readlane_b32 s68, v255, 11
	v_readlane_b32 s70, v255, 14
	v_readlane_b32 s71, v255, 15
	s_cbranch_execz .LBB0_2805
	s_lshl_b32 s24, s48, 10
	s_add_i32 s24, s28, s24
	s_waitcnt lgkmcnt(0)
	v_add_f32_e32 v168, v168, v169
	v_lshl_add_u32 v169, v166, 4, s24
	ds_write_b32 v169, v168

.LBB0_2898:
	s_lshl_b32 s4, s53, 5
	s_lshl_b32 s24, s20, 8
	v_lshrrev_b32_e32 v122, 1, v0
	s_or_b32 s4, s24, s4
	v_and_or_b32 v220, v122, 24, s4
	s_lshl_b32 s27, s52, 8
	v_add_u32_e32 v222, s27, v224
	v_ashrrev_i32_e32 v221, 31, v220
	v_lshl_add_u64 v[122:123], v[220:221], 1, s[22:23]
	s_mov_b64 s[22:23], 0x1bc00000
	v_ashrrev_i32_e32 v223, 31, v222
	v_lshl_add_u64 v[122:123], v[122:123], 0, s[22:23]
	v_lshlrev_b64 v[124:125], 11, v[222:223]
	v_lshl_add_u64 v[124:125], v[122:123], 0, v[124:125]
	s_barrier
	v_and_b32_e32 v168, 64, v231
	v_xor_b32_e32 v167, 16, v231
	v_add_u32_e32 v168, 64, v168
	v_cmp_lt_i32_e32 vcc, v167, v168
	v_mul_f32_e32 v169, v137, v137
	v_fmac_f32_e32 v169, v136, v136
	v_cndmask_b32_e32 v167, v231, v167, vcc
	v_lshlrev_b32_e32 v225, 2, v167
	v_mul_f32_e32 v167, v135, v135
	v_fmac_f32_e32 v167, v134, v134
	v_add_f32_e32 v167, v167, v169
	v_mul_f32_e32 v169, v131, v131
	v_mul_f32_e32 v170, v133, v133
	v_fmac_f32_e32 v169, v130, v130
	v_fmac_f32_e32 v170, v132, v132
	v_add_f32_e32 v169, v169, v170
	v_add_f32_e32 v167, v169, v167
	v_mul_f32_e32 v169, v119, v119
	v_mul_f32_e32 v170, v121, v121
	v_fmac_f32_e32 v169, v118, v118
	v_fmac_f32_e32 v170, v120, v120
	v_add_f32_e32 v169, v169, v170
	v_add_f32_e32 v167, v169, v167
	v_mul_f32_e32 v169, v115, v115
	v_mul_f32_e32 v170, v117, v117
	v_fmac_f32_e32 v169, v114, v114
	v_fmac_f32_e32 v170, v116, v116
	v_add_f32_e32 v169, v169, v170
	v_add_f32_e32 v167, v169, v167
	ds_bpermute_b32 v169, v225, v167
	v_xor_b32_e32 v170, 32, v231
	v_cmp_lt_i32_e32 vcc, v170, v168
	s_lshl_b32 s4, s53, 2
	s_add_i32 s26, s4, 0
	v_cndmask_b32_e32 v168, v231, v170, vcc
	v_lshlrev_b32_e32 v240, 2, v168
	s_waitcnt lgkmcnt(0)
	v_add_f32_e32 v167, v167, v169
	ds_bpermute_b32 v169, v240, v167
	v_and_b32_e32 v168, 63, v0
	v_cmp_gt_u32_e64 s[40:41], 16, v168
	s_and_saveexec_b64 s[22:23], s[40:41]
	v_readlane_b32 s64, v252, 3
	v_readlane_b32 s65, v255, 10
	v_readlane_b32 s68, v255, 11
	v_readlane_b32 s70, v255, 14
	v_readlane_b32 s71, v255, 15
	s_cbranch_execz .LBB0_2900
	s_lshl_b32 s4, s49, 10
	s_add_i32 s4, s26, s4
	s_waitcnt lgkmcnt(0)
	v_add_f32_e32 v167, v167, v169
	v_lshl_add_u32 v169, v166, 4, s4
	ds_write_b32 v169, v167

.LBB0_2919:
	s_or_b64 exec, exec, s[20:21]
	global_load_dwordx4 v[206:209], v[124:125], off
	global_load_dwordx4 v[202:205], v[124:125], off offset:256
	v_or_b32_e32 v124, 16, v222
	v_ashrrev_i32_e32 v125, 31, v124
	v_lshlrev_b64 v[124:125], 11, v[124:125]
	v_lshl_add_u64 v[124:125], v[122:123], 0, v[124:125]
	global_load_dwordx4 v[198:201], v[124:125], off
	global_load_dwordx4 v[194:197], v[124:125], off offset:256
	v_or_b32_e32 v124, 32, v222
	v_ashrrev_i32_e32 v125, 31, v124
	v_lshlrev_b64 v[124:125], 11, v[124:125]
	v_lshl_add_u64 v[124:125], v[122:123], 0, v[124:125]
	global_load_dwordx4 v[190:193], v[124:125], off
	global_load_dwordx4 v[186:189], v[124:125], off offset:256
	v_or_b32_e32 v124, 48, v222
	v_ashrrev_i32_e32 v125, 31, v124
	v_lshlrev_b64 v[124:125], 11, v[124:125]
	v_lshl_add_u64 v[124:125], v[122:123], 0, v[124:125]
	global_load_dwordx4 v[174:177], v[124:125], off
	global_load_dwordx4 v[162:165], v[124:125], off offset:256
	v_add_u32_e32 v124, 0x80, v222
	v_ashrrev_i32_e32 v125, 31, v124
	v_lshlrev_b64 v[124:125], 11, v[124:125]
	v_lshl_add_u64 v[124:125], v[122:123], 0, v[124:125]
	global_load_dwordx4 v[158:161], v[124:125], off
	global_load_dwordx4 v[154:157], v[124:125], off offset:256
	v_add_u32_e32 v124, 0x90, v222
	v_ashrrev_i32_e32 v125, 31, v124
	v_lshlrev_b64 v[124:125], 11, v[124:125]
	v_lshl_add_u64 v[124:125], v[122:123], 0, v[124:125]
	global_load_dwordx4 v[150:153], v[124:125], off
	global_load_dwordx4 v[146:149], v[124:125], off offset:256
	v_add_u32_e32 v124, 0xa0, v222
	v_ashrrev_i32_e32 v125, 31, v124
	v_lshlrev_b64 v[124:125], 11, v[124:125]
	v_lshl_add_u64 v[124:125], v[122:123], 0, v[124:125]
	global_load_dwordx4 v[142:145], v[124:125], off
	global_load_dwordx4 v[138:141], v[124:125], off offset:256
	v_add_u32_e32 v124, 0xb0, v222
	v_ashrrev_i32_e32 v125, 31, v124
	v_lshlrev_b64 v[124:125], 11, v[124:125]
	v_lshl_add_u64 v[122:123], v[122:123], 0, v[124:125]
	global_load_dwordx4 v[126:129], v[122:123], off
	s_nop 0
	global_load_dwordx4 v[122:125], v[122:123], off offset:256
	s_cmp_gt_u32 s48, 63
	s_cbranch_scc1 .LBB0_2936
	s_memrealtime s[20:21]
	s_branch .LBB0_2923

.LBB0_2989:
	s_lshl_b32 s24, s48, 5
	s_lshl_b32 s25, s20, 8
	v_lshrrev_b32_e32 v122, 1, v239
	s_add_i32 s4, s78, 64
	s_or_b32 s24, s25, s24
	v_and_or_b32 v220, v122, 24, s24
	s_lshl_b32 s27, s4, 8
	v_add_u32_e32 v222, s27, v224
	v_ashrrev_i32_e32 v221, 31, v220
	v_lshl_add_u64 v[122:123], v[220:221], 1, s[22:23]
	s_mov_b64 s[22:23], 0x1bc00000
	v_ashrrev_i32_e32 v223, 31, v222
	v_lshl_add_u64 v[122:123], v[122:123], 0, s[22:23]
	v_lshlrev_b64 v[124:125], 11, v[222:223]
	v_lshl_add_u64 v[124:125], v[122:123], 0, v[124:125]
	s_barrier
	v_and_b32_e32 v167, 64, v231
	v_xor_b32_e32 v166, 16, v231
	v_add_u32_e32 v167, 64, v167
	v_cmp_lt_i32_e32 vcc, v166, v167
	v_mul_f32_e32 v168, v137, v137
	v_fmac_f32_e32 v168, v136, v136
	v_cndmask_b32_e32 v166, v231, v166, vcc
	v_lshlrev_b32_e32 v225, 2, v166
	v_mul_f32_e32 v166, v135, v135
	v_fmac_f32_e32 v166, v134, v134
	v_add_f32_e32 v166, v166, v168
	v_mul_f32_e32 v168, v131, v131
	v_mul_f32_e32 v169, v133, v133
	v_fmac_f32_e32 v168, v130, v130
	v_fmac_f32_e32 v169, v132, v132
	v_add_f32_e32 v168, v168, v169
	v_add_f32_e32 v166, v168, v166
	v_mul_f32_e32 v168, v119, v119
	v_mul_f32_e32 v169, v121, v121
	v_fmac_f32_e32 v168, v118, v118
	v_fmac_f32_e32 v169, v120, v120
	v_add_f32_e32 v168, v168, v169
	v_add_f32_e32 v166, v168, v166
	v_mul_f32_e32 v168, v115, v115
	v_mul_f32_e32 v169, v117, v117
	v_fmac_f32_e32 v168, v114, v114
	v_fmac_f32_e32 v169, v116, v116
	v_add_f32_e32 v168, v168, v169
	v_add_f32_e32 v166, v168, v166
	ds_bpermute_b32 v168, v225, v166
	v_xor_b32_e32 v169, 32, v231
	v_cmp_lt_i32_e32 vcc, v169, v167
	s_lshl_b32 s22, s48, 2
	s_add_i32 s26, s22, 0
	v_cndmask_b32_e32 v167, v231, v169, vcc
	v_lshlrev_b32_e32 v240, 2, v167
	s_waitcnt lgkmcnt(0)
	v_add_f32_e32 v166, v166, v168
	ds_bpermute_b32 v167, v240, v166
	v_and_b32_e32 v168, 63, v239
	v_cmp_gt_u32_e64 s[38:39], 16, v168
	s_and_saveexec_b64 s[22:23], s[38:39]
	v_readlane_b32 s64, v252, 3
	v_readlane_b32 s65, v255, 10
	v_readlane_b32 s68, v255, 11
	s_cbranch_execz .LBB0_2991
	s_lshl_b32 s24, s47, 10
	s_add_i32 s24, s26, s24
	s_waitcnt lgkmcnt(0)
	v_add_f32_e32 v166, v166, v167
	v_lshl_add_u32 v167, v0, 4, s24
	ds_write_b32 v167, v166

.LBB0_3010:
	s_or_b64 exec, exec, s[20:21]
	global_load_dwordx4 v[206:209], v[124:125], off
	global_load_dwordx4 v[202:205], v[124:125], off offset:256
	v_or_b32_e32 v124, 16, v222
	v_ashrrev_i32_e32 v125, 31, v124
	v_lshlrev_b64 v[124:125], 11, v[124:125]
	v_lshl_add_u64 v[124:125], v[122:123], 0, v[124:125]
	global_load_dwordx4 v[198:201], v[124:125], off
	global_load_dwordx4 v[194:197], v[124:125], off offset:256
	v_or_b32_e32 v124, 32, v222
	v_ashrrev_i32_e32 v125, 31, v124
	v_lshlrev_b64 v[124:125], 11, v[124:125]
	v_lshl_add_u64 v[124:125], v[122:123], 0, v[124:125]
	global_load_dwordx4 v[190:193], v[124:125], off
	global_load_dwordx4 v[186:189], v[124:125], off offset:256
	v_or_b32_e32 v124, 48, v222
	v_ashrrev_i32_e32 v125, 31, v124
	v_lshlrev_b64 v[124:125], 11, v[124:125]
	v_lshl_add_u64 v[124:125], v[122:123], 0, v[124:125]
	global_load_dwordx4 v[174:177], v[124:125], off
	global_load_dwordx4 v[162:165], v[124:125], off offset:256
	v_add_u32_e32 v124, 0x80, v222
	v_ashrrev_i32_e32 v125, 31, v124
	v_lshlrev_b64 v[124:125], 11, v[124:125]
	v_lshl_add_u64 v[124:125], v[122:123], 0, v[124:125]
	global_load_dwordx4 v[158:161], v[124:125], off
	global_load_dwordx4 v[154:157], v[124:125], off offset:256
	v_add_u32_e32 v124, 0x90, v222
	v_ashrrev_i32_e32 v125, 31, v124
	v_lshlrev_b64 v[124:125], 11, v[124:125]
	v_lshl_add_u64 v[124:125], v[122:123], 0, v[124:125]
	global_load_dwordx4 v[150:153], v[124:125], off
	global_load_dwordx4 v[146:149], v[124:125], off offset:256
	v_add_u32_e32 v124, 0xa0, v222
	v_ashrrev_i32_e32 v125, 31, v124
	v_lshlrev_b64 v[124:125], 11, v[124:125]
	v_lshl_add_u64 v[124:125], v[122:123], 0, v[124:125]
	global_load_dwordx4 v[142:145], v[124:125], off
	global_load_dwordx4 v[138:141], v[124:125], off offset:256
	v_add_u32_e32 v124, 0xb0, v222
	v_ashrrev_i32_e32 v125, 31, v124
	v_lshlrev_b64 v[124:125], 11, v[124:125]
	v_lshl_add_u64 v[122:123], v[122:123], 0, v[124:125]
	global_load_dwordx4 v[126:129], v[122:123], off
	s_nop 0
	global_load_dwordx4 v[122:125], v[122:123], off offset:256
	s_cmp_gt_u32 s46, 63
	s_cbranch_scc1 .LBB0_3027
	s_memrealtime s[20:21]
	s_branch .LBB0_3014
